# all weight-conversion loops: per-set load waits (true 2-deep pipeline); 700 conversion blocks per layer moved from the mixer phase to the in_proj spare workgroups
# baseline (speedup 1.0000x reference)
.LBB0_310:
	s_lshl_b32 s4, s2, 3
	v_writelane_b32 v254, s4, 7
	s_lshl_b32 s4, s3, 3
	v_writelane_b32 v254, s4, 8
	s_lshl_b32 s4, s2, 9
	s_lshl_b32 s62, s3, 9
	s_cmp_eq_u32 s2, 0
	v_writelane_b32 v254, s4, 9
	s_cselect_b64 s[4:5], -1, 0
	v_writelane_b32 v254, s4, 10
	s_lshl_b32 s8, s2, 5
	s_and_b32 s14, s87, 31
	v_writelane_b32 v254, s5, 11
	s_mul_i32 s4, s2, 0x6b
	s_add_i32 s7, s4, 0xffffd954
	s_ashr_i32 s11, s87, 5
	s_lshl_b32 s4, s2, 4
	s_lshl_b32 s66, s3, 4
	s_cmpk_lt_i32 s2, 0x100
	v_writelane_b32 v254, s4, 12
	s_cselect_b64 s[4:5], -1, 0
	v_writelane_b32 v254, s4, 13
	s_movk_i32 s64, 0x80
	s_movk_i32 s65, 0xff00
	v_writelane_b32 v254, s5, 14
	s_not_b32 s4, s2
	s_add_i32 s4, s3, s4
	s_cmpk_lt_i32 s4, 0x80
	v_writelane_b32 v254, s4, 15
	s_cselect_b64 s[4:5], -1, 0
	s_and_b32 s9, s87, 3
	v_writelane_b32 v254, s4, 16
	s_cmpk_lt_i32 s2, 0x200
	s_movk_i32 s56, 0x1000
	v_writelane_b32 v254, s5, 17
	s_cselect_b64 s[4:5], -1, 0
	v_writelane_b32 v254, s4, 18
	s_lshl_b32 s74, s3, 5
	s_movk_i32 s77, 0x4400
	v_writelane_b32 v254, s5, 19
	s_lshl_b32 s4, s2, 2
	s_and_b32 s4, s4, 0xffffff00
	v_writelane_b32 v254, s4, 20
	s_lshl_b32 s4, s2, 6
	s_and_b32 s6, s4, 0xfc0
	s_cmp_gt_i32 s3, 0
	v_writelane_b32 v254, s4, 21
	s_cselect_b64 s[4:5], -1, 0
	v_writelane_b32 v254, s4, 22
	s_ashr_i32 s12, s87, 2
	s_mov_b32 s10, s12
	v_writelane_b32 v254, s5, 23
	s_ashr_i32 s4, s87, 3
	v_writelane_b32 v254, s4, 24
	s_and_b32 s5, s87, 7
	s_lshl_b32 s4, s5, 7
	v_writelane_b32 v254, s5, 25
	s_lshl_b32 s5, s5, 18
	v_writelane_b32 v254, s5, 26
	s_ashr_i32 s13, s12, 31
	v_writelane_b32 v254, s10, 27
	s_lshl_b64 s[12:13], s[12:13], 18
	s_lshl_b32 s5, s9, 8
	v_writelane_b32 v254, s11, 28
	v_writelane_b32 v254, s12, 29
	s_mov_b32 s38, 0x78787879
	s_movk_i32 s39, 0xef00
	v_writelane_b32 v254, s13, 30
	v_writelane_b32 v254, s9, 31
	s_lshl_b32 s9, s9, 18
	s_cmpk_lt_i32 s2, 0x84
	v_writelane_b32 v254, s9, 32
	s_cselect_b32 s9, 32, 0x6b
	v_writelane_b32 v254, s9, 33
	v_writelane_b32 v254, s8, 34
	s_cselect_b32 s7, s8, s7
	v_writelane_b32 v254, s7, 35
	s_add_i32 s7, s3, -1
	s_cmp_gt_u32 s7, 6
	s_cselect_b64 s[8:9], -1, 0
	s_abs_i32 s12, s3
	v_cvt_f32_u32_e32 v1, s12
	v_writelane_b32 v254, s8, 36
	s_sub_i32 s7, 0, s12
	s_and_b32 s76, s3, 0x7ffffff8
	v_rcp_iflag_f32_e32 v1, v1
	v_writelane_b32 v254, s9, 37
	s_ashr_i32 s13, s3, 31
	s_mov_b32 s59, 0x800000
	v_mul_f32_e32 v1, 0x4f7ffffe, v1
	v_cvt_u32_f32_e32 v1, v1
	v_mov_b32_e32 v205, 1
	v_mov_b32_e32 v221, 0x1400
	v_mov_b32_e32 v204, 0x20200
	v_readfirstlane_b32 s8, v1
	s_mul_i32 s7, s7, s8
	s_mul_hi_u32 s7, s8, s7
	s_add_i32 s7, s8, s7
	v_writelane_b32 v254, s7, 38
	s_mul_hi_u32 s7, s7, 0x4df
	s_mul_i32 s8, s7, s12
	s_sub_i32 s8, 0x4df, s8
	s_add_i32 s9, s7, 1
	s_sub_i32 s10, s8, s12
	s_cmp_ge_u32 s8, s12
	s_cselect_b32 s7, s9, s7
	s_cselect_b32 s8, s10, s8
	s_add_i32 s9, s7, 1
	s_cmp_ge_u32 s8, s12
	s_cselect_b32 s7, s9, s7
	s_xor_b32 s7, s7, s13
	s_sub_i32 s7, s7, s13
	s_mul_i32 s8, s7, s3
	s_sub_i32 s8, 0x4df, s8
	s_mul_i32 s9, s7, s87
	s_min_i32 s10, s87, s8
	v_writelane_b32 v254, s12, 39
	s_add_i32 s9, s9, s10
	v_writelane_b32 v254, s13, 40
	s_cmp_lt_i32 s87, s8
	v_writelane_b32 v254, s9, 41
	s_cselect_b64 s[8:9], -1, 0
	s_cmp_lg_u64 s[8:9], 0
	s_addc_u32 s7, s7, 0
	v_writelane_b32 v254, s7, 42
	s_lshl_b32 s7, s3, 1
	v_writelane_b32 v254, s7, 43
	s_add_i32 s7, s11, 17
	v_writelane_b32 v254, s7, 44
	s_lshl_b32 s7, s7, 4
	v_writelane_b32 v254, s7, 45
	s_lshl_b32 s7, s14, 4
	v_writelane_b32 v254, s14, 46
	s_add_i32 s8, s7, 0xd250
	v_writelane_b32 v254, s8, 47
	s_add_i32 s8, s11, 9
	v_writelane_b32 v254, s8, 48
	s_lshl_b32 s8, s8, 4
	v_writelane_b32 v254, s8, 49
	v_writelane_b32 v254, s11, 50
	s_add_i32 s8, s11, 1
	v_writelane_b32 v254, s8, 51
	s_or_b32 s8, s7, 0xfffffe00
	v_writelane_b32 v254, s8, 52
	s_lshl_b32 s8, s3, 6
	v_writelane_b32 v254, s8, 53
	s_add_i32 s7, s7, 0xa050
	v_writelane_b32 v254, s7, 54
	s_add_i32 s7, 0, 0x12000
	v_writelane_b32 v254, s7, 55
	s_add_i32 s7, 0, 0x27020
	v_writelane_b32 v254, s7, 56
	s_add_i32 s7, 0, 0x27024
	v_writelane_b32 v254, s7, 57
	s_add_i32 s7, 0, 0x25000
	v_writelane_b32 v254, s7, 58
	s_lshl_b32 s6, s6, 1
	v_writelane_b32 v254, s6, 59
	s_lshl_b32 s5, s5, 2
	v_writelane_b32 v254, s5, 60
	s_add_i32 s5, 0, 0x25400
	v_writelane_b32 v254, s5, 61
	s_add_i32 s5, 0, 0x10200
	v_writelane_b32 v254, s5, 62
	s_add_i32 s5, 0, 0x20100
	v_writelane_b32 v254, s5, 63
	s_add_i32 s5, 0, 0x20010
	v_writelane_b32 v255, s5, 0
	s_add_i32 s5, 0, 0x20110
	v_writelane_b32 v255, s5, 1
	s_add_i32 s5, 0, 0x20020
	v_writelane_b32 v255, s5, 2
	s_add_i32 s5, 0, 0x20120
	v_writelane_b32 v255, s5, 3
	s_add_i32 s5, 0, 0x20030
	v_writelane_b32 v255, s5, 4
	s_add_i32 s5, 0, 0x20130
	v_writelane_b32 v255, s5, 5
	s_add_i32 s5, 0, 0x20040
	v_writelane_b32 v255, s5, 6
	s_add_i32 s5, 0, 0x20140
	v_writelane_b32 v255, s5, 7
	s_add_i32 s5, 0, 0x20050
	v_writelane_b32 v255, s5, 8
	s_add_i32 s5, 0, 0x20150
	v_writelane_b32 v255, s5, 9
	s_add_i32 s5, 0, 0x20060
	v_writelane_b32 v255, s5, 10
	s_add_i32 s5, 0, 0x20160
	v_writelane_b32 v255, s5, 11
	s_add_i32 s5, 0, 0x20070
	v_writelane_b32 v255, s5, 12
	s_add_i32 s5, 0, 0x20170
	v_writelane_b32 v255, s5, 13
	s_add_i32 s5, 0, 0x20180
	v_writelane_b32 v255, s5, 14
	s_add_i32 s5, 0, 0x20084
	v_writelane_b32 v255, s5, 15
	s_add_i32 s5, 0, 0x20024
	v_writelane_b32 v255, s5, 16
	s_add_i32 s5, 0, 0x2002c
	v_writelane_b32 v255, s5, 17
	s_add_i32 s5, 0, 0x20034
	v_writelane_b32 v255, s5, 18
	s_add_i32 s5, 0, 0x2003c
	v_writelane_b32 v255, s5, 19
	s_add_i32 s5, 0, 0x20044
	v_writelane_b32 v255, s5, 20
	s_add_i32 s5, 0, 0x2004c
	v_writelane_b32 v255, s5, 21
	s_add_i32 s5, 0, 0x20054
	v_writelane_b32 v255, s5, 22
	s_add_i32 s5, 0, 0x2005c
	v_writelane_b32 v255, s5, 23
	s_add_i32 s5, 0, 0x20064
	v_writelane_b32 v255, s5, 24
	s_add_i32 s5, 0, 0x2006c
	v_writelane_b32 v255, s5, 25
	s_add_i32 s5, 0, 0x20074
	v_writelane_b32 v255, s5, 26
	s_add_i32 s5, 0, 0x2007c
	v_writelane_b32 v255, s5, 27
	s_add_i32 s5, 0, 0x20800
	v_writelane_b32 v255, s5, 28
	s_lshl_b32 s4, s4, 2
	v_writelane_b32 v255, s4, 29
	s_ashr_i32 s63, s62, 31
	s_ashr_i32 s67, s66, 31
	v_writelane_b32 v255, s5, 30
	v_cmp_eq_u32_e64 s[4:5], 0, v0
	s_mov_b32 s6, s74
	s_add_i32 s84, 0, 0x20004
	v_writelane_b32 v255, s4, 31
	s_add_i32 s69, 0, 0x2000c
	s_add_i32 s68, 0, 0x20014
	v_writelane_b32 v255, s5, 32
	s_lshl_b64 s[4:5], s[62:63], 2
	v_writelane_b32 v255, s4, 33
	s_add_i32 s49, 0, 0x2001c
	v_mov_b32_e32 v1, 0
	v_writelane_b32 v255, s5, 34
	s_lshl_b64 s[4:5], s[66:67], 12
	v_writelane_b32 v255, s4, 35
	v_mov_b32_e32 v220, 0xff800000
	s_movk_i32 s47, 0x3ff
	v_writelane_b32 v255, s5, 36
	v_writelane_b32 v255, s6, 37
	s_mov_b32 s83, 0x34400000
	s_mov_b32 s80, 0x36500000
	v_writelane_b32 v255, s7, 38
	s_mov_b32 s6, s62
	v_writelane_b32 v255, s6, 39
	s_movk_i32 s81, 0x7fff
	s_mov_b32 s57, 0x41000000
	v_writelane_b32 v255, s7, 40
	s_mov_b32 s6, s66
	v_writelane_b32 v255, s6, 41
	s_movk_i32 s33, 0xfefe
	s_mov_b32 s85, 0x900000
	v_writelane_b32 v255, s7, 42
	v_writelane_b32 v255, s76, 43
	v_writelane_b32 v255, s84, 44
	s_mov_b32 s72, 0xc0e00000
	s_mov_b32 s73, 0
	s_mov_b32 s71, 0
	s_mov_b64 s[4:5], -1
	s_mov_b64 s[78:79], 0x80
	s_mov_b32 s82, 0x3e38aa3b
	s_mov_b32 s88, 0xc01d265f
	s_mov_b32 s50, s69
	s_mov_b32 s86, s68
	s_mov_b32 s60, s49
	v_writelane_b32 v255, s87, 45
	s_branch .LBB0_314

.LBB0_561:
	s_and_b64 vcc, exec, s[16:17]
	s_cbranch_vccz .LBB0_711
	v_readlane_b32 s6, v254, 50
	v_readlane_b32 s7, v254, 46
	s_mul_i32 s6, s35, s6
	s_sub_i32 s7, s7, s36
	s_add_i32 s23, s7, s6
	s_lshl_b32 s22, s35, 3
	s_mov_b64 s[6:7], -1
	s_and_b64 vcc, exec, s[90:91]
	s_cbranch_vccz .LBB0_637
	v_mbcnt_lo_u32_b32 v66, -1, 0
	v_mbcnt_hi_u32_b32 v66, -1, v66
	s_getreg_b32 s6, hwreg(HW_REG_HW_ID, 0, 6)
	s_lshl_b32 s6, s6, 2
	s_and_b32 s6, s6, 0xfc
	s_or_b32 s6, s6, 0x27100
	v_mov_b32_e32 v0, s6
	ds_read_b32 v0, v0
	s_cmpk_gt_i32 s23, 0x5db
	s_waitcnt lgkmcnt(0)
	v_readfirstlane_b32 s9, v0
	s_cbranch_scc1 .LBB0_636
	s_add_i32 s20, s23, 0xd45
	s_mul_hi_i32 s6, s20, 0x2aaaaaab
	s_lshr_b32 s7, s6, 31
	s_ashr_i32 s15, s6, 9
	s_add_i32 s15, s15, s7
	s_mul_i32 s16, s15, 0xfffff400
	s_add_i32 s16, s16, s20
	s_cmpk_gt_i32 s16, 0x7ff
	s_mov_b64 s[12:13], -1
	s_cbranch_scc0 .LBB0_566
	s_add_i32 s6, s16, 0xfffff800
	s_mov_b32 s10, 31
	s_lshl_b32 s7, s15, 5
	s_lshr_b32 s6, s6, 5
	s_lshl_b32 s24, s20, 8
	s_ashr_i32 s11, s10, 31
	s_add_i32 s6, s6, s7
	s_lshl_b32 s14, s20, 5
	s_and_b32 s8, s24, 0x300
	s_lshl_b64 s[10:11], s[10:11], 3
	s_add_u32 s10, s0, s10
	s_addc_u32 s11, s1, s11
	s_load_dwordx2 s[10:11], s[10:11], 0x0
	s_ashr_i32 s7, s6, 31
	s_lshl_b64 s[12:13], s[6:7], 20
	s_lshl_b64 s[6:7], s[6:7], 22
	s_waitcnt lgkmcnt(0)
	s_add_u32 s6, s10, s6
	s_mov_b32 s10, 35
	s_addc_u32 s7, s11, s7
	s_ashr_i32 s11, s10, 31
	s_lshl_b64 s[10:11], s[10:11], 3
	s_add_u32 s10, s0, s10
	s_addc_u32 s11, s1, s11
	s_load_dwordx2 s[10:11], s[10:11], 0x0
	s_waitcnt lgkmcnt(0)
	s_add_u32 s10, s10, s12
	s_addc_u32 s11, s11, s13
	s_add_u32 s10, s10, 0x12800000
	s_addc_u32 s11, s11, 0
	s_mov_b64 s[12:13], 0

.LBB0_571:
	v_ashrrev_i32_e32 v139, 31, v138
	v_lshlrev_b64 v[138:139], 10, v[138:139]
	s_add_i32 s30, s30, s27
	v_readlane_b32 s6, v254, 46
	v_lshl_add_u64 v[138:139], s[16:17], 0, v[138:139]
	s_add_i32 s24, s24, s25
	s_add_i32 s26, s26, s27
	s_add_i32 s36, s36, s28
	s_add_i32 s29, s29, s27
	s_add_i32 s6, s6, s30
	v_lshl_add_u64 v[138:139], v[138:139], 0, s[14:15]
	s_cmpk_gt_i32 s6, 0x1320
	v_lshl_add_u64 v[138:139], v[138:139], 0, v[136:137]
	s_cselect_b64 s[6:7], -1, 0
	s_waitcnt lgkmcnt(0)
	global_store_dwordx4 v[138:139], v[130:133], off

.LBB0_573:
	v_readlane_b32 s6, v254, 46
	s_add_i32 s6, s6, s29
	s_add_i32 s9, s20, s22
	s_add_i32 s7, s6, 0xd25
	s_cmpk_lt_i32 s7, 0x1321
	s_cselect_b64 s[18:19], -1, 0
	s_cmpk_gt_i32 s7, 0x1320
	s_cbranch_scc1 .LBB0_580
	s_mul_hi_i32 s7, s7, 0x2aaaaaab
	s_lshr_b32 s12, s7, 31
	s_ashr_i32 s20, s7, 9
	s_add_i32 s20, s20, s12
	s_mul_i32 s7, s20, 0xfffff400
	s_add_i32 s37, s6, s7
	s_add_i32 s21, s37, 0xd25
	s_cmpk_gt_i32 s21, 0x7ff
	s_mov_b64 s[14:15], -1
	s_cbranch_scc0 .LBB0_576
	s_addk_i32 s37, 0x525
	s_mov_b32 s14, 31
	s_lshl_b32 s6, s20, 5
	s_lshr_b32 s7, s37, 5
	s_ashr_i32 s15, s14, 31
	s_add_i32 s6, s7, s6
	s_lshl_b32 s13, s9, 5
	s_and_b32 s12, s24, 0x300
	s_lshl_b64 s[14:15], s[14:15], 3
	s_add_u32 s14, s0, s14
	s_addc_u32 s15, s1, s15
	s_load_dwordx2 s[14:15], s[14:15], 0x0
	s_ashr_i32 s7, s6, 31
	s_lshl_b64 s[16:17], s[6:7], 20
	s_lshl_b64 s[6:7], s[6:7], 22
	s_waitcnt lgkmcnt(0)
	s_add_u32 s6, s14, s6
	s_mov_b32 s14, 35
	s_addc_u32 s7, s15, s7
	s_ashr_i32 s15, s14, 31
	s_lshl_b64 s[14:15], s[14:15], 3
	s_add_u32 s14, s0, s14
	s_addc_u32 s15, s1, s15
	s_load_dwordx2 s[14:15], s[14:15], 0x0
	s_waitcnt lgkmcnt(0)
	s_add_u32 s14, s14, s16
	s_addc_u32 s15, s15, s17
	s_add_u32 s16, s14, 0x12800000
	s_addc_u32 s17, s15, 0
	s_mov_b64 s[14:15], 0

.LBB0_579:
	s_and_b32 s14, s13, 0x380
	v_add_u32_e32 v0, s14, v135
	v_mad_i64_i32 v[66:67], s[40:41], s20, v0, 0
	v_lshl_add_u64 v[66:67], v[66:67], 2, s[6:7]
	s_mov_b32 s13, s71
	v_lshl_add_u64 v[66:67], s[12:13], 2, v[66:67]
	v_lshlrev_b32_e32 v0, 2, v134
	v_lshl_add_u64 v[66:67], v[66:67], 0, v[0:1]
	s_lshl_b32 s6, s20, 2
	s_mov_b32 s7, s71
	v_lshl_add_u64 v[74:75], v[66:67], 0, s[6:7]
	global_load_dwordx4 v[70:73], v[66:67], off nt
	s_nop 0
	global_load_dwordx4 v[66:69], v[74:75], off nt
	v_lshl_add_u64 v[74:75], v[74:75], 0, s[6:7]
	v_lshl_add_u64 v[82:83], v[74:75], 0, s[6:7]
	global_load_dwordx4 v[78:81], v[74:75], off nt
	s_nop 0
	global_load_dwordx4 v[74:77], v[82:83], off nt
	v_lshl_add_u64 v[82:83], v[82:83], 0, s[6:7]
	v_lshl_add_u64 v[90:91], v[82:83], 0, s[6:7]
	global_load_dwordx4 v[86:89], v[82:83], off nt
	s_nop 0
	global_load_dwordx4 v[82:85], v[90:91], off nt
	v_lshl_add_u64 v[90:91], v[90:91], 0, s[6:7]
	v_lshl_add_u64 v[98:99], v[90:91], 0, s[6:7]
	v_lshl_add_u64 v[102:103], v[98:99], 0, s[6:7]
	v_lshl_add_u64 v[106:107], v[102:103], 0, s[6:7]
	v_lshl_add_u64 v[110:111], v[106:107], 0, s[6:7]
	v_lshl_add_u64 v[114:115], v[110:111], 0, s[6:7]
	v_lshl_add_u64 v[118:119], v[114:115], 0, s[6:7]
	v_lshl_add_u64 v[122:123], v[118:119], 0, s[6:7]
	v_lshl_add_u64 v[126:127], v[122:123], 0, s[6:7]
	global_load_dwordx4 v[94:97], v[90:91], off nt
	s_nop 0
	global_load_dwordx4 v[90:93], v[98:99], off nt
	s_nop 0
	global_load_dwordx4 v[98:101], v[102:103], off nt
	s_nop 0
	global_load_dwordx4 v[102:105], v[106:107], off nt
	s_nop 0
	global_load_dwordx4 v[106:109], v[110:111], off nt
	s_nop 0
	global_load_dwordx4 v[110:113], v[114:115], off nt
	s_nop 0
	global_load_dwordx4 v[114:117], v[118:119], off nt
	s_nop 0
	global_load_dwordx4 v[118:121], v[122:123], off nt
	s_nop 0
	global_load_dwordx4 v[122:125], v[126:127], off nt
	v_lshl_add_u64 v[126:127], v[126:127], 0, s[6:7]
	global_load_dwordx4 v[126:129], v[126:127], off nt
	s_waitcnt vmcnt(16)
	s_branch .Lcvp0_a_ready

.Lcvp0_a_ready:
	v_mul_f32_e32 v0, 0x42800000, v2
	v_mul_f32_e32 v131, 0x42800000, v6
	v_mov_b32_e32 v130, v1
	v_cvt_pk_fp8_f32 v130, v0, v131
	v_mul_f32_e32 v132, 0x42800000, v10
	v_mul_f32_e32 v133, 0x42800000, v14
	v_mul_f32_e32 v0, 0x42800000, v18
	v_cvt_pk_fp8_f32 v130, v132, v133 op_sel:[0,0,1]
	v_mul_f32_e32 v132, 0x42800000, v22
	v_mov_b32_e32 v131, v1
	v_cvt_pk_fp8_f32 v131, v0, v132
	v_mul_f32_e32 v133, 0x42800000, v26
	v_mul_f32_e32 v138, 0x42800000, v30
	v_mul_f32_e32 v0, 0x42800000, v34
	v_cvt_pk_fp8_f32 v131, v133, v138 op_sel:[0,0,1]
	v_mul_f32_e32 v133, 0x42800000, v38
	v_mov_b32_e32 v132, v1
	v_cvt_pk_fp8_f32 v132, v0, v133
	v_mul_f32_e32 v138, 0x42800000, v42
	v_mul_f32_e32 v139, 0x42800000, v46
	v_mul_f32_e32 v0, 0x42800000, v50
	v_cvt_pk_fp8_f32 v132, v138, v139 op_sel:[0,0,1]
	v_mul_f32_e32 v138, 0x42800000, v54
	v_mov_b32_e32 v133, v1
	v_cvt_pk_fp8_f32 v133, v0, v138
	v_mul_f32_e32 v139, 0x42800000, v58
	v_mul_f32_e32 v149, 0x42800000, v62
	v_mul_f32_e32 v0, 0x42800000, v3
	v_cvt_pk_fp8_f32 v133, v139, v149 op_sel:[0,0,1]
	v_mul_f32_e32 v138, 0x42800000, v31
	v_mul_f32_e32 v139, 0x42800000, v47
	v_mul_f32_e32 v149, 0x42800000, v63
	ds_write_b128 v144, v[130:133]
	v_mul_f32_e32 v131, 0x42800000, v7
	v_mov_b32_e32 v130, v1
	v_cvt_pk_fp8_f32 v130, v0, v131
	v_mul_f32_e32 v132, 0x42800000, v11
	v_mul_f32_e32 v133, 0x42800000, v15
	v_mul_f32_e32 v0, 0x42800000, v19
	v_cvt_pk_fp8_f32 v130, v132, v133 op_sel:[0,0,1]
	v_mul_f32_e32 v132, 0x42800000, v23
	v_mov_b32_e32 v131, v1
	v_cvt_pk_fp8_f32 v131, v0, v132
	v_mul_f32_e32 v133, 0x42800000, v27
	v_mul_f32_e32 v0, 0x42800000, v35
	v_mov_b32_e32 v132, v1
	v_cvt_pk_fp8_f32 v131, v133, v138 op_sel:[0,0,1]
	v_mul_f32_e32 v133, 0x42800000, v39
	v_cvt_pk_fp8_f32 v132, v0, v133
	v_mul_f32_e32 v138, 0x42800000, v43
	v_mul_f32_e32 v0, 0x42800000, v51
	v_mov_b32_e32 v133, v1
	v_cvt_pk_fp8_f32 v132, v138, v139 op_sel:[0,0,1]
	v_mul_f32_e32 v138, 0x42800000, v55
	v_cvt_pk_fp8_f32 v133, v0, v138
	v_mul_f32_e32 v139, 0x42800000, v59
	v_mul_f32_e32 v0, 0x42800000, v4
	v_mul_f32_e32 v138, 0x42800000, v32
	v_cvt_pk_fp8_f32 v133, v139, v149 op_sel:[0,0,1]
	v_mul_f32_e32 v139, 0x42800000, v48
	v_mul_f32_e32 v149, 0x42800000, v64
	s_cmp_lg_u32 s31, 0
	ds_write_b128 v144, v[130:133] offset:128
	v_mul_f32_e32 v131, 0x42800000, v8
	v_mov_b32_e32 v130, v1
	v_cvt_pk_fp8_f32 v130, v0, v131
	v_mul_f32_e32 v132, 0x42800000, v12
	v_mul_f32_e32 v133, 0x42800000, v16
	v_mul_f32_e32 v0, 0x42800000, v20
	v_cvt_pk_fp8_f32 v130, v132, v133 op_sel:[0,0,1]
	v_mul_f32_e32 v132, 0x42800000, v24
	v_mov_b32_e32 v131, v1
	v_cvt_pk_fp8_f32 v131, v0, v132
	v_mul_f32_e32 v133, 0x42800000, v28
	v_mul_f32_e32 v0, 0x42800000, v36
	v_mov_b32_e32 v132, v1
	v_cvt_pk_fp8_f32 v131, v133, v138 op_sel:[0,0,1]
	v_mul_f32_e32 v133, 0x42800000, v40
	v_cvt_pk_fp8_f32 v132, v0, v133
	v_mul_f32_e32 v138, 0x42800000, v44
	v_mul_f32_e32 v0, 0x42800000, v52
	v_mov_b32_e32 v133, v1
	v_cvt_pk_fp8_f32 v132, v138, v139 op_sel:[0,0,1]
	v_mul_f32_e32 v138, 0x42800000, v56
	v_cvt_pk_fp8_f32 v133, v0, v138
	v_mul_f32_e32 v139, 0x42800000, v60
	v_mul_f32_e32 v0, 0x42800000, v5
	v_mul_f32_e32 v138, 0x42800000, v33
	v_cvt_pk_fp8_f32 v133, v139, v149 op_sel:[0,0,1]
	v_mul_f32_e32 v139, 0x42800000, v49
	v_mul_f32_e32 v149, 0x42800000, v65
	s_cselect_b64 s[20:21], -1, 0
	ds_write_b128 v144, v[130:133] offset:256
	v_mul_f32_e32 v131, 0x42800000, v9
	v_mov_b32_e32 v130, v1
	v_cvt_pk_fp8_f32 v130, v0, v131
	v_mul_f32_e32 v132, 0x42800000, v13
	v_mul_f32_e32 v133, 0x42800000, v17
	v_mul_f32_e32 v0, 0x42800000, v21
	v_cvt_pk_fp8_f32 v130, v132, v133 op_sel:[0,0,1]
	v_mul_f32_e32 v132, 0x42800000, v25
	v_mov_b32_e32 v131, v1
	v_cvt_pk_fp8_f32 v131, v0, v132
	v_mul_f32_e32 v133, 0x42800000, v29
	v_mul_f32_e32 v0, 0x42800000, v37
	v_mov_b32_e32 v132, v1
	v_cvt_pk_fp8_f32 v131, v133, v138 op_sel:[0,0,1]
	v_mul_f32_e32 v133, 0x42800000, v41
	v_cvt_pk_fp8_f32 v132, v0, v133
	v_mul_f32_e32 v138, 0x42800000, v45
	v_mul_f32_e32 v0, 0x42800000, v53
	v_mov_b32_e32 v133, v1
	v_cvt_pk_fp8_f32 v132, v138, v139 op_sel:[0,0,1]
	v_mul_f32_e32 v138, 0x42800000, v57
	v_cvt_pk_fp8_f32 v133, v0, v138
	v_mul_f32_e32 v139, 0x42800000, v61
	v_add_u32_e32 v138, s8, v140
	s_cmp_eq_u32 s31, 0
	v_cvt_pk_fp8_f32 v133, v139, v149 op_sel:[0,0,1]
	ds_write_b128 v144, v[130:133] offset:384
	s_waitcnt lgkmcnt(0)
	s_barrier
	ds_read_b128 v[130:133], v145
	s_cbranch_scc1 .LBB0_586
	v_cmp_lt_i32_e32 vcc, s47, v138
	v_lshlrev_b32_e32 v0, 1, v138
	v_and_b32_e32 v139, 0x7f, v138
	s_and_saveexec_b64 s[6:7], vcc
	s_xor_b64 s[6:7], exec, s[6:7]
	v_add_u32_e32 v0, 0x7ffff800, v0
	v_and_b32_e32 v0, 0x7fffff00, v0
	v_or3_b32 v138, v139, v0, s64
	s_andn2_saveexec_b64 s[6:7], s[6:7]
	v_and_or_b32 v138, v0, s65, v139
	s_or_b64 exec, exec, s[6:7]

.LBB0_604:
	v_ashrrev_i32_e32 v139, 31, v138
	v_lshlrev_b64 v[138:139], 10, v[138:139]
	v_lshl_add_u64 v[138:139], s[10:11], 0, v[138:139]
	v_lshl_add_u64 v[138:139], v[138:139], 0, s[70:71]
	v_lshl_add_u64 v[138:139], v[138:139], 0, v[136:137]
	s_andn2_b64 vcc, exec, s[18:19]
	s_mov_b64 s[6:7], -1
	s_waitcnt lgkmcnt(0)
	global_store_dwordx4 v[138:139], v[130:133], off
	s_cbranch_vccnz .LBB0_572
	v_readlane_b32 s6, v254, 46
	s_add_i32 s6, s6, s26
	s_add_i32 s20, s9, s22
	s_add_i32 s7, s6, 0xd25
	s_cmpk_gt_i32 s7, 0x1320
	s_cbranch_scc1 .LBB0_612
	s_mul_hi_i32 s7, s7, 0x2aaaaaab
	s_lshr_b32 s8, s7, 31
	s_ashr_i32 s13, s7, 9
	s_add_i32 s13, s13, s8
	s_mul_i32 s7, s13, 0xfffff400
	s_add_i32 s21, s6, s7
	s_add_i32 s15, s21, 0xd25
	s_cmpk_gt_i32 s15, 0x7ff
	s_mov_b64 s[18:19], -1
	s_cbranch_scc0 .LBB0_608
	s_addk_i32 s21, 0x525
	s_mov_b32 s10, 31
	s_lshl_b32 s6, s13, 5
	s_lshr_b32 s7, s21, 5
	s_ashr_i32 s11, s10, 31
	s_add_i32 s6, s7, s6
	s_lshl_b32 s9, s20, 5
	s_and_b32 s8, s24, 0x300
	s_lshl_b64 s[10:11], s[10:11], 3
	s_add_u32 s10, s0, s10
	s_addc_u32 s11, s1, s11
	s_load_dwordx2 s[10:11], s[10:11], 0x0
	s_ashr_i32 s7, s6, 31
	s_lshl_b64 s[18:19], s[6:7], 20
	s_lshl_b64 s[6:7], s[6:7], 22
	s_waitcnt lgkmcnt(0)
	s_add_u32 s6, s10, s6
	s_mov_b32 s10, 35
	s_addc_u32 s7, s11, s7
	s_ashr_i32 s11, s10, 31
	s_lshl_b64 s[10:11], s[10:11], 3
	s_add_u32 s10, s0, s10
	s_addc_u32 s11, s1, s11
	s_load_dwordx2 s[10:11], s[10:11], 0x0
	s_waitcnt lgkmcnt(0)
	s_add_u32 s10, s10, s18
	s_addc_u32 s11, s11, s19
	s_add_u32 s10, s10, 0x12800000
	s_addc_u32 s11, s11, 0
	s_mov_b64 s[18:19], 0

.LBB0_611:
	s_and_b32 s13, s9, 0x380
	v_add_u32_e32 v0, s13, v135
	v_mad_i64_i32 v[2:3], s[40:41], s18, v0, 0
	v_lshl_add_u64 v[2:3], v[2:3], 2, s[6:7]
	s_mov_b32 s9, s71
	v_lshl_add_u64 v[2:3], s[8:9], 2, v[2:3]
	v_lshlrev_b32_e32 v0, 2, v134
	v_lshl_add_u64 v[2:3], v[2:3], 0, v[0:1]
	s_lshl_b32 s70, s18, 2
	v_lshl_add_u64 v[10:11], v[2:3], 0, s[70:71]
	global_load_dwordx4 v[2:5], v[2:3], off nt
	s_nop 0
	global_load_dwordx4 v[6:9], v[10:11], off nt
	v_lshl_add_u64 v[10:11], v[10:11], 0, s[70:71]
	v_lshl_add_u64 v[18:19], v[10:11], 0, s[70:71]
	global_load_dwordx4 v[10:13], v[10:11], off nt
	s_nop 0
	global_load_dwordx4 v[14:17], v[18:19], off nt
	v_lshl_add_u64 v[18:19], v[18:19], 0, s[70:71]
	v_lshl_add_u64 v[26:27], v[18:19], 0, s[70:71]
	global_load_dwordx4 v[18:21], v[18:19], off nt
	s_nop 0
	global_load_dwordx4 v[22:25], v[26:27], off nt
	v_lshl_add_u64 v[26:27], v[26:27], 0, s[70:71]
	v_lshl_add_u64 v[34:35], v[26:27], 0, s[70:71]
	v_lshl_add_u64 v[38:39], v[34:35], 0, s[70:71]
	v_lshl_add_u64 v[42:43], v[38:39], 0, s[70:71]
	v_lshl_add_u64 v[46:47], v[42:43], 0, s[70:71]
	v_lshl_add_u64 v[50:51], v[46:47], 0, s[70:71]
	v_lshl_add_u64 v[54:55], v[50:51], 0, s[70:71]
	v_lshl_add_u64 v[58:59], v[54:55], 0, s[70:71]
	v_lshl_add_u64 v[62:63], v[58:59], 0, s[70:71]
	global_load_dwordx4 v[26:29], v[26:27], off nt
	s_nop 0
	global_load_dwordx4 v[30:33], v[34:35], off nt
	s_nop 0
	global_load_dwordx4 v[34:37], v[38:39], off nt
	s_nop 0
	global_load_dwordx4 v[38:41], v[42:43], off nt
	s_nop 0
	global_load_dwordx4 v[42:45], v[46:47], off nt
	s_nop 0
	global_load_dwordx4 v[46:49], v[50:51], off nt
	s_nop 0
	global_load_dwordx4 v[50:53], v[54:55], off nt
	s_nop 0
	global_load_dwordx4 v[54:57], v[58:59], off nt
	s_nop 0
	global_load_dwordx4 v[58:61], v[62:63], off nt
	v_lshl_add_u64 v[62:63], v[62:63], 0, s[70:71]
	global_load_dwordx4 v[62:65], v[62:63], off nt
	s_mov_b32 s70, s13
	s_waitcnt vmcnt(16)
	s_branch .Lcvp0_b_ready
.LBB0_612:
	s_waitcnt vmcnt(0)
.Lcvp0_b_ready:
	v_mul_f32_e32 v0, 0x42800000, v70
	v_mul_f32_e32 v131, 0x42800000, v66
	v_mov_b32_e32 v130, v1
	v_cvt_pk_fp8_f32 v130, v0, v131
	v_mul_f32_e32 v132, 0x42800000, v78
	v_mul_f32_e32 v133, 0x42800000, v74
	v_mul_f32_e32 v0, 0x42800000, v86
	v_cvt_pk_fp8_f32 v130, v132, v133 op_sel:[0,0,1]
	v_mul_f32_e32 v132, 0x42800000, v82
	v_mov_b32_e32 v131, v1
	v_cvt_pk_fp8_f32 v131, v0, v132
	v_mul_f32_e32 v133, 0x42800000, v94
	v_mul_f32_e32 v138, 0x42800000, v90
	v_mul_f32_e32 v0, 0x42800000, v98
	v_cvt_pk_fp8_f32 v131, v133, v138 op_sel:[0,0,1]
	v_mul_f32_e32 v133, 0x42800000, v102
	v_mov_b32_e32 v132, v1
	v_cvt_pk_fp8_f32 v132, v0, v133
	v_mul_f32_e32 v138, 0x42800000, v106
	v_mul_f32_e32 v139, 0x42800000, v110
	v_mul_f32_e32 v0, 0x42800000, v114
	v_cvt_pk_fp8_f32 v132, v138, v139 op_sel:[0,0,1]
	v_mul_f32_e32 v138, 0x42800000, v118
	v_mov_b32_e32 v133, v1
	v_cvt_pk_fp8_f32 v133, v0, v138
	v_mul_f32_e32 v139, 0x42800000, v122
	v_mul_f32_e32 v149, 0x42800000, v126
	v_mul_f32_e32 v0, 0x42800000, v71
	v_cvt_pk_fp8_f32 v133, v139, v149 op_sel:[0,0,1]
	v_mul_f32_e32 v138, 0x42800000, v91
	v_mul_f32_e32 v139, 0x42800000, v111
	v_mul_f32_e32 v149, 0x42800000, v127
	ds_write_b128 v144, v[130:133] offset:32768
	v_mul_f32_e32 v131, 0x42800000, v67
	v_mov_b32_e32 v130, v1
	v_cvt_pk_fp8_f32 v130, v0, v131
	v_mul_f32_e32 v132, 0x42800000, v79
	v_mul_f32_e32 v133, 0x42800000, v75
	v_mul_f32_e32 v0, 0x42800000, v87
	v_cvt_pk_fp8_f32 v130, v132, v133 op_sel:[0,0,1]
	v_mul_f32_e32 v132, 0x42800000, v83
	v_mov_b32_e32 v131, v1
	v_cvt_pk_fp8_f32 v131, v0, v132
	v_mul_f32_e32 v133, 0x42800000, v95
	v_mul_f32_e32 v0, 0x42800000, v99
	v_mov_b32_e32 v132, v1
	v_cvt_pk_fp8_f32 v131, v133, v138 op_sel:[0,0,1]
	v_mul_f32_e32 v133, 0x42800000, v103
	v_cvt_pk_fp8_f32 v132, v0, v133
	v_mul_f32_e32 v138, 0x42800000, v107
	v_mul_f32_e32 v0, 0x42800000, v115
	v_mov_b32_e32 v133, v1
	v_cvt_pk_fp8_f32 v132, v138, v139 op_sel:[0,0,1]
	v_mul_f32_e32 v138, 0x42800000, v119
	v_cvt_pk_fp8_f32 v133, v0, v138
	v_mul_f32_e32 v139, 0x42800000, v123
	v_mul_f32_e32 v0, 0x42800000, v72
	v_mul_f32_e32 v138, 0x42800000, v92
	v_cvt_pk_fp8_f32 v133, v139, v149 op_sel:[0,0,1]
	v_mul_f32_e32 v139, 0x42800000, v112
	v_mul_f32_e32 v149, 0x42800000, v128
	s_cmp_lg_u32 s37, 0
	ds_write_b128 v144, v[130:133] offset:32896
	v_mul_f32_e32 v131, 0x42800000, v68
	v_mov_b32_e32 v130, v1
	v_cvt_pk_fp8_f32 v130, v0, v131
	v_mul_f32_e32 v132, 0x42800000, v80
	v_mul_f32_e32 v133, 0x42800000, v76
	v_mul_f32_e32 v0, 0x42800000, v88
	v_cvt_pk_fp8_f32 v130, v132, v133 op_sel:[0,0,1]
	v_mul_f32_e32 v132, 0x42800000, v84
	v_mov_b32_e32 v131, v1
	v_cvt_pk_fp8_f32 v131, v0, v132
	v_mul_f32_e32 v133, 0x42800000, v96
	v_mul_f32_e32 v0, 0x42800000, v100
	v_mov_b32_e32 v132, v1
	v_cvt_pk_fp8_f32 v131, v133, v138 op_sel:[0,0,1]
	v_mul_f32_e32 v133, 0x42800000, v104
	v_cvt_pk_fp8_f32 v132, v0, v133
	v_mul_f32_e32 v138, 0x42800000, v108
	v_mul_f32_e32 v0, 0x42800000, v116
	v_mov_b32_e32 v133, v1
	v_cvt_pk_fp8_f32 v132, v138, v139 op_sel:[0,0,1]
	v_mul_f32_e32 v138, 0x42800000, v120
	v_cvt_pk_fp8_f32 v133, v0, v138
	v_mul_f32_e32 v139, 0x42800000, v124
	v_mul_f32_e32 v0, 0x42800000, v73
	v_mul_f32_e32 v138, 0x42800000, v93
	v_cvt_pk_fp8_f32 v133, v139, v149 op_sel:[0,0,1]
	v_mul_f32_e32 v139, 0x42800000, v113
	v_mul_f32_e32 v149, 0x42800000, v129
	s_cselect_b64 s[18:19], -1, 0
	ds_write_b128 v144, v[130:133] offset:33024
	v_mul_f32_e32 v131, 0x42800000, v69
	v_mov_b32_e32 v130, v1
	v_cvt_pk_fp8_f32 v130, v0, v131
	v_mul_f32_e32 v132, 0x42800000, v81
	v_mul_f32_e32 v133, 0x42800000, v77
	v_mul_f32_e32 v0, 0x42800000, v89
	v_cvt_pk_fp8_f32 v130, v132, v133 op_sel:[0,0,1]
	v_mul_f32_e32 v132, 0x42800000, v85
	v_mov_b32_e32 v131, v1
	v_cvt_pk_fp8_f32 v131, v0, v132
	v_mul_f32_e32 v133, 0x42800000, v97
	v_mul_f32_e32 v0, 0x42800000, v101
	v_mov_b32_e32 v132, v1
	v_cvt_pk_fp8_f32 v131, v133, v138 op_sel:[0,0,1]
	v_mul_f32_e32 v133, 0x42800000, v105
	v_cvt_pk_fp8_f32 v132, v0, v133
	v_mul_f32_e32 v138, 0x42800000, v109
	v_mul_f32_e32 v0, 0x42800000, v117
	v_mov_b32_e32 v133, v1
	v_cvt_pk_fp8_f32 v132, v138, v139 op_sel:[0,0,1]
	v_mul_f32_e32 v138, 0x42800000, v121
	v_cvt_pk_fp8_f32 v133, v0, v138
	v_mul_f32_e32 v139, 0x42800000, v125
	v_add_u32_e32 v138, s12, v140
	s_cmp_eq_u32 s37, 0
	v_cvt_pk_fp8_f32 v133, v139, v149 op_sel:[0,0,1]
	ds_write_b128 v144, v[130:133] offset:33152
	s_waitcnt lgkmcnt(0)
	s_barrier
	ds_read_b128 v[130:133], v145 offset:32768
	s_cbranch_scc1 .LBB0_618
	v_cmp_lt_i32_e32 vcc, s47, v138
	v_lshlrev_b32_e32 v0, 1, v138
	v_and_b32_e32 v139, 0x7f, v138
	s_and_saveexec_b64 s[6:7], vcc
	s_xor_b64 s[6:7], exec, s[6:7]
	v_add_u32_e32 v0, 0x7ffff800, v0
	v_and_b32_e32 v0, 0x7fffff00, v0
	v_or3_b32 v138, v139, v0, s64
	s_andn2_saveexec_b64 s[6:7], s[6:7]
	v_and_or_b32 v138, v0, s65, v139
	s_or_b64 exec, exec, s[6:7]

.LBB0_637:
	s_andn2_b64 vcc, exec, s[6:7]
	s_cbranch_vccnz .LBB0_711
	v_mbcnt_lo_u32_b32 v66, -1, 0
	v_mbcnt_hi_u32_b32 v66, -1, v66
	s_getreg_b32 s6, hwreg(HW_REG_HW_ID, 0, 6)
	s_lshl_b32 s6, s6, 2
	s_and_b32 s6, s6, 0xfc
	s_or_b32 s6, s6, 0x27100
	v_mov_b32_e32 v0, s6
	ds_read_b32 v0, v0
	s_cmpk_gt_i32 s23, 0x545
	s_waitcnt lgkmcnt(0)
	v_readfirstlane_b32 s9, v0
	s_cbranch_scc1 .LBB0_711
	s_mul_hi_i32 s6, s23, 0x2aaaaaab
	s_lshr_b32 s7, s6, 31
	s_ashr_i32 s15, s6, 9
	s_add_i32 s15, s15, s7
	s_mul_i32 s16, s15, 0xfffff400
	s_add_i32 s16, s16, s23
	s_cmpk_gt_i32 s16, 0x7ff
	s_mov_b64 s[12:13], -1
	s_cbranch_scc0 .LBB0_641
	s_add_i32 s6, s16, 0xfffff800
	s_mov_b32 s10, 31
	s_lshl_b32 s7, s15, 5
	s_lshr_b32 s6, s6, 5
	s_lshl_b32 s24, s23, 8
	s_ashr_i32 s11, s10, 31
	s_add_i32 s6, s6, s7
	s_lshl_b32 s14, s23, 5
	s_and_b32 s8, s24, 0x300
	s_lshl_b64 s[10:11], s[10:11], 3
	s_add_u32 s10, s0, s10
	s_addc_u32 s11, s1, s11
	s_load_dwordx2 s[10:11], s[10:11], 0x0
	s_ashr_i32 s7, s6, 31
	s_lshl_b64 s[12:13], s[6:7], 20
	s_lshl_b64 s[6:7], s[6:7], 22
	s_waitcnt lgkmcnt(0)
	s_add_u32 s6, s10, s6
	s_mov_b32 s10, 35
	s_addc_u32 s7, s11, s7
	s_ashr_i32 s11, s10, 31
	s_lshl_b64 s[10:11], s[10:11], 3
	s_add_u32 s10, s0, s10
	s_addc_u32 s11, s1, s11
	s_load_dwordx2 s[10:11], s[10:11], 0x0
	s_waitcnt lgkmcnt(0)
	s_add_u32 s10, s10, s12
	s_addc_u32 s11, s11, s13
	s_add_u32 s10, s10, 0x12800000
	s_addc_u32 s11, s11, 0
	s_mov_b64 s[12:13], 0

.LBB0_646:
	v_ashrrev_i32_e32 v139, 31, v138
	v_lshlrev_b64 v[138:139], 10, v[138:139]
	s_add_i32 s35, s35, s27
	v_readlane_b32 s6, v254, 46
	v_lshl_add_u64 v[138:139], s[16:17], 0, v[138:139]
	s_add_i32 s24, s24, s25
	s_add_i32 s26, s26, s27
	s_add_i32 s37, s37, s29
	s_add_i32 s30, s30, s27
	s_add_i32 s6, s6, s35
	v_lshl_add_u64 v[138:139], v[138:139], 0, s[14:15]
	s_cmpk_gt_i32 s6, 0x545
	v_lshl_add_u64 v[138:139], v[138:139], 0, v[136:137]
	s_cselect_b64 s[6:7], -1, 0
	s_waitcnt lgkmcnt(0)
	global_store_dwordx4 v[138:139], v[130:133], off

.LBB0_648:
	v_readlane_b32 s6, v254, 46
	s_add_i32 s6, s6, s30
	s_add_i32 s9, s23, s22
	s_sub_i32 s7, s6, 32
	s_cmpk_lt_i32 s7, 0x546
	s_cselect_b64 s[18:19], -1, 0
	s_cmpk_gt_i32 s7, 0x545
	s_cbranch_scc1 .LBB0_655
	s_mul_hi_i32 s7, s7, 0x2aaaaaab
	s_lshr_b32 s12, s7, 31
	s_ashr_i32 s20, s7, 9
	s_add_i32 s20, s20, s12
	s_mul_i32 s7, s20, 0xfffff400
	s_add_i32 s23, s6, s7
	s_sub_i32 s21, s23, 32
	s_cmpk_gt_i32 s21, 0x7ff
	s_mov_b64 s[14:15], -1
	s_cbranch_scc0 .LBB0_651
	s_addk_i32 s23, 0xf7e0
	s_mov_b32 s14, 31
	s_lshl_b32 s6, s20, 5
	s_lshr_b32 s7, s23, 5
	s_ashr_i32 s15, s14, 31
	s_add_i32 s6, s7, s6
	s_lshl_b32 s13, s9, 5
	s_and_b32 s12, s24, 0x300
	s_lshl_b64 s[14:15], s[14:15], 3
	s_add_u32 s14, s0, s14
	s_addc_u32 s15, s1, s15
	s_load_dwordx2 s[14:15], s[14:15], 0x0
	s_ashr_i32 s7, s6, 31
	s_lshl_b64 s[16:17], s[6:7], 20
	s_lshl_b64 s[6:7], s[6:7], 22
	s_waitcnt lgkmcnt(0)
	s_add_u32 s6, s14, s6
	s_mov_b32 s14, 35
	s_addc_u32 s7, s15, s7
	s_ashr_i32 s15, s14, 31
	s_lshl_b64 s[14:15], s[14:15], 3
	s_add_u32 s14, s0, s14
	s_addc_u32 s15, s1, s15
	s_load_dwordx2 s[14:15], s[14:15], 0x0
	s_waitcnt lgkmcnt(0)
	s_add_u32 s14, s14, s16
	s_addc_u32 s15, s15, s17
	s_add_u32 s16, s14, 0x12800000
	s_addc_u32 s17, s15, 0
	s_mov_b64 s[14:15], 0

.LBB0_654:
	s_and_b32 s14, s13, 0x380
	v_add_u32_e32 v0, s14, v135
	v_mad_i64_i32 v[66:67], s[42:43], s20, v0, 0
	v_lshl_add_u64 v[66:67], v[66:67], 2, s[6:7]
	s_mov_b32 s13, s71
	v_lshl_add_u64 v[66:67], s[12:13], 2, v[66:67]
	v_lshlrev_b32_e32 v0, 2, v134
	v_lshl_add_u64 v[66:67], v[66:67], 0, v[0:1]
	s_lshl_b32 s6, s20, 2
	s_mov_b32 s7, s71
	v_lshl_add_u64 v[74:75], v[66:67], 0, s[6:7]
	global_load_dwordx4 v[70:73], v[66:67], off nt
	s_nop 0
	global_load_dwordx4 v[66:69], v[74:75], off nt
	v_lshl_add_u64 v[74:75], v[74:75], 0, s[6:7]
	v_lshl_add_u64 v[82:83], v[74:75], 0, s[6:7]
	global_load_dwordx4 v[78:81], v[74:75], off nt
	s_nop 0
	global_load_dwordx4 v[74:77], v[82:83], off nt
	v_lshl_add_u64 v[82:83], v[82:83], 0, s[6:7]
	v_lshl_add_u64 v[90:91], v[82:83], 0, s[6:7]
	global_load_dwordx4 v[86:89], v[82:83], off nt
	s_nop 0
	global_load_dwordx4 v[82:85], v[90:91], off nt
	v_lshl_add_u64 v[90:91], v[90:91], 0, s[6:7]
	v_lshl_add_u64 v[98:99], v[90:91], 0, s[6:7]
	v_lshl_add_u64 v[102:103], v[98:99], 0, s[6:7]
	v_lshl_add_u64 v[106:107], v[102:103], 0, s[6:7]
	v_lshl_add_u64 v[110:111], v[106:107], 0, s[6:7]
	v_lshl_add_u64 v[114:115], v[110:111], 0, s[6:7]
	v_lshl_add_u64 v[118:119], v[114:115], 0, s[6:7]
	v_lshl_add_u64 v[122:123], v[118:119], 0, s[6:7]
	v_lshl_add_u64 v[126:127], v[122:123], 0, s[6:7]
	global_load_dwordx4 v[94:97], v[90:91], off nt
	s_nop 0
	global_load_dwordx4 v[90:93], v[98:99], off nt
	s_nop 0
	global_load_dwordx4 v[98:101], v[102:103], off nt
	s_nop 0
	global_load_dwordx4 v[102:105], v[106:107], off nt
	s_nop 0
	global_load_dwordx4 v[106:109], v[110:111], off nt
	s_nop 0
	global_load_dwordx4 v[110:113], v[114:115], off nt
	s_nop 0
	global_load_dwordx4 v[114:117], v[118:119], off nt
	s_nop 0
	global_load_dwordx4 v[118:121], v[122:123], off nt
	s_nop 0
	global_load_dwordx4 v[122:125], v[126:127], off nt
	v_lshl_add_u64 v[126:127], v[126:127], 0, s[6:7]
	global_load_dwordx4 v[126:129], v[126:127], off nt
	s_waitcnt vmcnt(16)
	s_branch .Lcvp1_a_ready

.Lcvp1_a_ready:
	v_mul_f32_e32 v0, 0x42800000, v2
	v_mul_f32_e32 v131, 0x42800000, v6
	v_mov_b32_e32 v130, v1
	v_cvt_pk_fp8_f32 v130, v0, v131
	v_mul_f32_e32 v132, 0x42800000, v10
	v_mul_f32_e32 v133, 0x42800000, v14
	v_mul_f32_e32 v0, 0x42800000, v18
	v_cvt_pk_fp8_f32 v130, v132, v133 op_sel:[0,0,1]
	v_mul_f32_e32 v132, 0x42800000, v22
	v_mov_b32_e32 v131, v1
	v_cvt_pk_fp8_f32 v131, v0, v132
	v_mul_f32_e32 v133, 0x42800000, v26
	v_mul_f32_e32 v138, 0x42800000, v30
	v_mul_f32_e32 v0, 0x42800000, v34
	v_cvt_pk_fp8_f32 v131, v133, v138 op_sel:[0,0,1]
	v_mul_f32_e32 v133, 0x42800000, v38
	v_mov_b32_e32 v132, v1
	v_cvt_pk_fp8_f32 v132, v0, v133
	v_mul_f32_e32 v138, 0x42800000, v42
	v_mul_f32_e32 v139, 0x42800000, v46
	v_mul_f32_e32 v0, 0x42800000, v50
	v_cvt_pk_fp8_f32 v132, v138, v139 op_sel:[0,0,1]
	v_mul_f32_e32 v138, 0x42800000, v54
	v_mov_b32_e32 v133, v1
	v_cvt_pk_fp8_f32 v133, v0, v138
	v_mul_f32_e32 v139, 0x42800000, v58
	v_mul_f32_e32 v149, 0x42800000, v62
	v_mul_f32_e32 v0, 0x42800000, v3
	v_cvt_pk_fp8_f32 v133, v139, v149 op_sel:[0,0,1]
	v_mul_f32_e32 v138, 0x42800000, v31
	v_mul_f32_e32 v139, 0x42800000, v47
	v_mul_f32_e32 v149, 0x42800000, v63
	ds_write_b128 v144, v[130:133]
	v_mul_f32_e32 v131, 0x42800000, v7
	v_mov_b32_e32 v130, v1
	v_cvt_pk_fp8_f32 v130, v0, v131
	v_mul_f32_e32 v132, 0x42800000, v11
	v_mul_f32_e32 v133, 0x42800000, v15
	v_mul_f32_e32 v0, 0x42800000, v19
	v_cvt_pk_fp8_f32 v130, v132, v133 op_sel:[0,0,1]
	v_mul_f32_e32 v132, 0x42800000, v23
	v_mov_b32_e32 v131, v1
	v_cvt_pk_fp8_f32 v131, v0, v132
	v_mul_f32_e32 v133, 0x42800000, v27
	v_mul_f32_e32 v0, 0x42800000, v35
	v_mov_b32_e32 v132, v1
	v_cvt_pk_fp8_f32 v131, v133, v138 op_sel:[0,0,1]
	v_mul_f32_e32 v133, 0x42800000, v39
	v_cvt_pk_fp8_f32 v132, v0, v133
	v_mul_f32_e32 v138, 0x42800000, v43
	v_mul_f32_e32 v0, 0x42800000, v51
	v_mov_b32_e32 v133, v1
	v_cvt_pk_fp8_f32 v132, v138, v139 op_sel:[0,0,1]
	v_mul_f32_e32 v138, 0x42800000, v55
	v_cvt_pk_fp8_f32 v133, v0, v138
	v_mul_f32_e32 v139, 0x42800000, v59
	v_mul_f32_e32 v0, 0x42800000, v4
	v_mul_f32_e32 v138, 0x42800000, v32
	v_cvt_pk_fp8_f32 v133, v139, v149 op_sel:[0,0,1]
	v_mul_f32_e32 v139, 0x42800000, v48
	v_mul_f32_e32 v149, 0x42800000, v64
	s_cmp_lg_u32 s36, 0
	ds_write_b128 v144, v[130:133] offset:128
	v_mul_f32_e32 v131, 0x42800000, v8
	v_mov_b32_e32 v130, v1
	v_cvt_pk_fp8_f32 v130, v0, v131
	v_mul_f32_e32 v132, 0x42800000, v12
	v_mul_f32_e32 v133, 0x42800000, v16
	v_mul_f32_e32 v0, 0x42800000, v20
	v_cvt_pk_fp8_f32 v130, v132, v133 op_sel:[0,0,1]
	v_mul_f32_e32 v132, 0x42800000, v24
	v_mov_b32_e32 v131, v1
	v_cvt_pk_fp8_f32 v131, v0, v132
	v_mul_f32_e32 v133, 0x42800000, v28
	v_mul_f32_e32 v0, 0x42800000, v36
	v_mov_b32_e32 v132, v1
	v_cvt_pk_fp8_f32 v131, v133, v138 op_sel:[0,0,1]
	v_mul_f32_e32 v133, 0x42800000, v40
	v_cvt_pk_fp8_f32 v132, v0, v133
	v_mul_f32_e32 v138, 0x42800000, v44
	v_mul_f32_e32 v0, 0x42800000, v52
	v_mov_b32_e32 v133, v1
	v_cvt_pk_fp8_f32 v132, v138, v139 op_sel:[0,0,1]
	v_mul_f32_e32 v138, 0x42800000, v56
	v_cvt_pk_fp8_f32 v133, v0, v138
	v_mul_f32_e32 v139, 0x42800000, v60
	v_mul_f32_e32 v0, 0x42800000, v5
	v_mul_f32_e32 v138, 0x42800000, v33
	v_cvt_pk_fp8_f32 v133, v139, v149 op_sel:[0,0,1]
	v_mul_f32_e32 v139, 0x42800000, v49
	v_mul_f32_e32 v149, 0x42800000, v65
	s_cselect_b64 s[20:21], -1, 0
	ds_write_b128 v144, v[130:133] offset:256
	v_mul_f32_e32 v131, 0x42800000, v9
	v_mov_b32_e32 v130, v1
	v_cvt_pk_fp8_f32 v130, v0, v131
	v_mul_f32_e32 v132, 0x42800000, v13
	v_mul_f32_e32 v133, 0x42800000, v17
	v_mul_f32_e32 v0, 0x42800000, v21
	v_cvt_pk_fp8_f32 v130, v132, v133 op_sel:[0,0,1]
	v_mul_f32_e32 v132, 0x42800000, v25
	v_mov_b32_e32 v131, v1
	v_cvt_pk_fp8_f32 v131, v0, v132
	v_mul_f32_e32 v133, 0x42800000, v29
	v_mul_f32_e32 v0, 0x42800000, v37
	v_mov_b32_e32 v132, v1
	v_cvt_pk_fp8_f32 v131, v133, v138 op_sel:[0,0,1]
	v_mul_f32_e32 v133, 0x42800000, v41
	v_cvt_pk_fp8_f32 v132, v0, v133
	v_mul_f32_e32 v138, 0x42800000, v45
	v_mul_f32_e32 v0, 0x42800000, v53
	v_mov_b32_e32 v133, v1
	v_cvt_pk_fp8_f32 v132, v138, v139 op_sel:[0,0,1]
	v_mul_f32_e32 v138, 0x42800000, v57
	v_cvt_pk_fp8_f32 v133, v0, v138
	v_mul_f32_e32 v139, 0x42800000, v61
	v_add_u32_e32 v138, s8, v140
	s_cmp_eq_u32 s36, 0
	v_cvt_pk_fp8_f32 v133, v139, v149 op_sel:[0,0,1]
	ds_write_b128 v144, v[130:133] offset:384
	s_waitcnt lgkmcnt(0)
	s_barrier
	ds_read_b128 v[130:133], v145
	s_cbranch_scc1 .LBB0_661
	v_cmp_lt_i32_e32 vcc, s47, v138
	v_lshlrev_b32_e32 v0, 1, v138
	v_and_b32_e32 v139, 0x7f, v138
	s_and_saveexec_b64 s[6:7], vcc
	s_xor_b64 s[6:7], exec, s[6:7]
	v_add_u32_e32 v0, 0x7ffff800, v0
	v_and_b32_e32 v0, 0x7fffff00, v0
	v_or3_b32 v138, v139, v0, s64
	s_andn2_saveexec_b64 s[6:7], s[6:7]
	v_and_or_b32 v138, v0, s65, v139
	s_or_b64 exec, exec, s[6:7]

.LBB0_679:
	v_ashrrev_i32_e32 v139, 31, v138
	v_lshlrev_b64 v[138:139], 10, v[138:139]
	v_lshl_add_u64 v[138:139], s[10:11], 0, v[138:139]
	v_lshl_add_u64 v[138:139], v[138:139], 0, s[70:71]
	v_lshl_add_u64 v[138:139], v[138:139], 0, v[136:137]
	s_andn2_b64 vcc, exec, s[18:19]
	s_mov_b64 s[6:7], -1
	s_waitcnt lgkmcnt(0)
	global_store_dwordx4 v[138:139], v[130:133], off
	s_cbranch_vccnz .LBB0_647
	v_readlane_b32 s6, v254, 46
	s_add_i32 s6, s6, s26
	s_add_i32 s23, s9, s22
	s_sub_i32 s7, s6, 32
	s_cmpk_gt_i32 s7, 0x545
	s_cbranch_scc1 .LBB0_687
	s_mul_hi_i32 s7, s7, 0x2aaaaaab
	s_lshr_b32 s8, s7, 31
	s_ashr_i32 s13, s7, 9
	s_add_i32 s13, s13, s8
	s_mul_i32 s7, s13, 0xfffff400
	s_add_i32 s20, s6, s7
	s_sub_i32 s15, s20, 32
	s_cmpk_gt_i32 s15, 0x7ff
	s_mov_b64 s[18:19], -1
	s_cbranch_scc0 .LBB0_683
	s_addk_i32 s20, 0xf7e0
	s_mov_b32 s10, 31
	s_lshl_b32 s6, s13, 5
	s_lshr_b32 s7, s20, 5
	s_ashr_i32 s11, s10, 31
	s_add_i32 s6, s7, s6
	s_lshl_b32 s9, s23, 5
	s_and_b32 s8, s24, 0x300
	s_lshl_b64 s[10:11], s[10:11], 3
	s_add_u32 s10, s0, s10
	s_addc_u32 s11, s1, s11
	s_load_dwordx2 s[10:11], s[10:11], 0x0
	s_ashr_i32 s7, s6, 31
	s_lshl_b64 s[18:19], s[6:7], 20
	s_lshl_b64 s[6:7], s[6:7], 22
	s_waitcnt lgkmcnt(0)
	s_add_u32 s6, s10, s6
	s_mov_b32 s10, 35
	s_addc_u32 s7, s11, s7
	s_ashr_i32 s11, s10, 31
	s_lshl_b64 s[10:11], s[10:11], 3
	s_add_u32 s10, s0, s10
	s_addc_u32 s11, s1, s11
	s_load_dwordx2 s[10:11], s[10:11], 0x0
	s_waitcnt lgkmcnt(0)
	s_add_u32 s10, s10, s18
	s_addc_u32 s11, s11, s19
	s_add_u32 s10, s10, 0x12800000
	s_addc_u32 s11, s11, 0
	s_mov_b64 s[18:19], 0

.LBB0_686:
	s_and_b32 s13, s9, 0x380
	v_add_u32_e32 v0, s13, v135
	v_mad_i64_i32 v[2:3], s[20:21], s18, v0, 0
	v_lshl_add_u64 v[2:3], v[2:3], 2, s[6:7]
	s_mov_b32 s9, s71
	v_lshl_add_u64 v[2:3], s[8:9], 2, v[2:3]
	v_lshlrev_b32_e32 v0, 2, v134
	v_lshl_add_u64 v[2:3], v[2:3], 0, v[0:1]
	s_lshl_b32 s70, s18, 2
	v_lshl_add_u64 v[10:11], v[2:3], 0, s[70:71]
	global_load_dwordx4 v[2:5], v[2:3], off nt
	s_nop 0
	global_load_dwordx4 v[6:9], v[10:11], off nt
	v_lshl_add_u64 v[10:11], v[10:11], 0, s[70:71]
	v_lshl_add_u64 v[18:19], v[10:11], 0, s[70:71]
	global_load_dwordx4 v[10:13], v[10:11], off nt
	s_nop 0
	global_load_dwordx4 v[14:17], v[18:19], off nt
	v_lshl_add_u64 v[18:19], v[18:19], 0, s[70:71]
	v_lshl_add_u64 v[26:27], v[18:19], 0, s[70:71]
	global_load_dwordx4 v[18:21], v[18:19], off nt
	s_nop 0
	global_load_dwordx4 v[22:25], v[26:27], off nt
	v_lshl_add_u64 v[26:27], v[26:27], 0, s[70:71]
	v_lshl_add_u64 v[34:35], v[26:27], 0, s[70:71]
	v_lshl_add_u64 v[38:39], v[34:35], 0, s[70:71]
	v_lshl_add_u64 v[42:43], v[38:39], 0, s[70:71]
	v_lshl_add_u64 v[46:47], v[42:43], 0, s[70:71]
	v_lshl_add_u64 v[50:51], v[46:47], 0, s[70:71]
	v_lshl_add_u64 v[54:55], v[50:51], 0, s[70:71]
	v_lshl_add_u64 v[58:59], v[54:55], 0, s[70:71]
	v_lshl_add_u64 v[62:63], v[58:59], 0, s[70:71]
	global_load_dwordx4 v[26:29], v[26:27], off nt
	s_nop 0
	global_load_dwordx4 v[30:33], v[34:35], off nt
	s_nop 0
	global_load_dwordx4 v[34:37], v[38:39], off nt
	s_nop 0
	global_load_dwordx4 v[38:41], v[42:43], off nt
	s_nop 0
	global_load_dwordx4 v[42:45], v[46:47], off nt
	s_nop 0
	global_load_dwordx4 v[46:49], v[50:51], off nt
	s_nop 0
	global_load_dwordx4 v[50:53], v[54:55], off nt
	s_nop 0
	global_load_dwordx4 v[54:57], v[58:59], off nt
	s_nop 0
	global_load_dwordx4 v[58:61], v[62:63], off nt
	v_lshl_add_u64 v[62:63], v[62:63], 0, s[70:71]
	global_load_dwordx4 v[62:65], v[62:63], off nt
	s_mov_b32 s70, s13
	s_waitcnt vmcnt(16)
	s_branch .Lcvp1_b_ready
.LBB0_687:
	s_waitcnt vmcnt(0)
.Lcvp1_b_ready:
	v_mul_f32_e32 v0, 0x42800000, v70
	v_mul_f32_e32 v131, 0x42800000, v66
	v_mov_b32_e32 v130, v1
	v_cvt_pk_fp8_f32 v130, v0, v131
	v_mul_f32_e32 v132, 0x42800000, v78
	v_mul_f32_e32 v133, 0x42800000, v74
	v_mul_f32_e32 v0, 0x42800000, v86
	v_cvt_pk_fp8_f32 v130, v132, v133 op_sel:[0,0,1]
	v_mul_f32_e32 v132, 0x42800000, v82
	v_mov_b32_e32 v131, v1
	v_cvt_pk_fp8_f32 v131, v0, v132
	v_mul_f32_e32 v133, 0x42800000, v94
	v_mul_f32_e32 v138, 0x42800000, v90
	v_mul_f32_e32 v0, 0x42800000, v98
	v_cvt_pk_fp8_f32 v131, v133, v138 op_sel:[0,0,1]
	v_mul_f32_e32 v133, 0x42800000, v102
	v_mov_b32_e32 v132, v1
	v_cvt_pk_fp8_f32 v132, v0, v133
	v_mul_f32_e32 v138, 0x42800000, v106
	v_mul_f32_e32 v139, 0x42800000, v110
	v_mul_f32_e32 v0, 0x42800000, v114
	v_cvt_pk_fp8_f32 v132, v138, v139 op_sel:[0,0,1]
	v_mul_f32_e32 v138, 0x42800000, v118
	v_mov_b32_e32 v133, v1
	v_cvt_pk_fp8_f32 v133, v0, v138
	v_mul_f32_e32 v139, 0x42800000, v122
	v_mul_f32_e32 v149, 0x42800000, v126
	v_mul_f32_e32 v0, 0x42800000, v71
	v_cvt_pk_fp8_f32 v133, v139, v149 op_sel:[0,0,1]
	v_mul_f32_e32 v138, 0x42800000, v91
	v_mul_f32_e32 v139, 0x42800000, v111
	v_mul_f32_e32 v149, 0x42800000, v127
	ds_write_b128 v144, v[130:133] offset:32768
	v_mul_f32_e32 v131, 0x42800000, v67
	v_mov_b32_e32 v130, v1
	v_cvt_pk_fp8_f32 v130, v0, v131
	v_mul_f32_e32 v132, 0x42800000, v79
	v_mul_f32_e32 v133, 0x42800000, v75
	v_mul_f32_e32 v0, 0x42800000, v87
	v_cvt_pk_fp8_f32 v130, v132, v133 op_sel:[0,0,1]
	v_mul_f32_e32 v132, 0x42800000, v83
	v_mov_b32_e32 v131, v1
	v_cvt_pk_fp8_f32 v131, v0, v132
	v_mul_f32_e32 v133, 0x42800000, v95
	v_mul_f32_e32 v0, 0x42800000, v99
	v_mov_b32_e32 v132, v1
	v_cvt_pk_fp8_f32 v131, v133, v138 op_sel:[0,0,1]
	v_mul_f32_e32 v133, 0x42800000, v103
	v_cvt_pk_fp8_f32 v132, v0, v133
	v_mul_f32_e32 v138, 0x42800000, v107
	v_mul_f32_e32 v0, 0x42800000, v115
	v_mov_b32_e32 v133, v1
	v_cvt_pk_fp8_f32 v132, v138, v139 op_sel:[0,0,1]
	v_mul_f32_e32 v138, 0x42800000, v119
	v_cvt_pk_fp8_f32 v133, v0, v138
	v_mul_f32_e32 v139, 0x42800000, v123
	v_mul_f32_e32 v0, 0x42800000, v72
	v_mul_f32_e32 v138, 0x42800000, v92
	v_cvt_pk_fp8_f32 v133, v139, v149 op_sel:[0,0,1]
	v_mul_f32_e32 v139, 0x42800000, v112
	v_mul_f32_e32 v149, 0x42800000, v128
	s_cmp_lg_u32 s40, 0
	ds_write_b128 v144, v[130:133] offset:32896
	v_mul_f32_e32 v131, 0x42800000, v68
	v_mov_b32_e32 v130, v1
	v_cvt_pk_fp8_f32 v130, v0, v131
	v_mul_f32_e32 v132, 0x42800000, v80
	v_mul_f32_e32 v133, 0x42800000, v76
	v_mul_f32_e32 v0, 0x42800000, v88
	v_cvt_pk_fp8_f32 v130, v132, v133 op_sel:[0,0,1]
	v_mul_f32_e32 v132, 0x42800000, v84
	v_mov_b32_e32 v131, v1
	v_cvt_pk_fp8_f32 v131, v0, v132
	v_mul_f32_e32 v133, 0x42800000, v96
	v_mul_f32_e32 v0, 0x42800000, v100
	v_mov_b32_e32 v132, v1
	v_cvt_pk_fp8_f32 v131, v133, v138 op_sel:[0,0,1]
	v_mul_f32_e32 v133, 0x42800000, v104
	v_cvt_pk_fp8_f32 v132, v0, v133
	v_mul_f32_e32 v138, 0x42800000, v108
	v_mul_f32_e32 v0, 0x42800000, v116
	v_mov_b32_e32 v133, v1
	v_cvt_pk_fp8_f32 v132, v138, v139 op_sel:[0,0,1]
	v_mul_f32_e32 v138, 0x42800000, v120
	v_cvt_pk_fp8_f32 v133, v0, v138
	v_mul_f32_e32 v139, 0x42800000, v124
	v_mul_f32_e32 v0, 0x42800000, v73
	v_mul_f32_e32 v138, 0x42800000, v93
	v_cvt_pk_fp8_f32 v133, v139, v149 op_sel:[0,0,1]
	v_mul_f32_e32 v139, 0x42800000, v113
	v_mul_f32_e32 v149, 0x42800000, v129
	s_cselect_b64 s[18:19], -1, 0
	ds_write_b128 v144, v[130:133] offset:33024
	v_mul_f32_e32 v131, 0x42800000, v69
	v_mov_b32_e32 v130, v1
	v_cvt_pk_fp8_f32 v130, v0, v131
	v_mul_f32_e32 v132, 0x42800000, v81
	v_mul_f32_e32 v133, 0x42800000, v77
	v_mul_f32_e32 v0, 0x42800000, v89
	v_cvt_pk_fp8_f32 v130, v132, v133 op_sel:[0,0,1]
	v_mul_f32_e32 v132, 0x42800000, v85
	v_mov_b32_e32 v131, v1
	v_cvt_pk_fp8_f32 v131, v0, v132
	v_mul_f32_e32 v133, 0x42800000, v97
	v_mul_f32_e32 v0, 0x42800000, v101
	v_mov_b32_e32 v132, v1
	v_cvt_pk_fp8_f32 v131, v133, v138 op_sel:[0,0,1]
	v_mul_f32_e32 v133, 0x42800000, v105
	v_cvt_pk_fp8_f32 v132, v0, v133
	v_mul_f32_e32 v138, 0x42800000, v109
	v_mul_f32_e32 v0, 0x42800000, v117
	v_mov_b32_e32 v133, v1
	v_cvt_pk_fp8_f32 v132, v138, v139 op_sel:[0,0,1]
	v_mul_f32_e32 v138, 0x42800000, v121
	v_cvt_pk_fp8_f32 v133, v0, v138
	v_mul_f32_e32 v139, 0x42800000, v125
	v_add_u32_e32 v138, s12, v140
	s_cmp_eq_u32 s40, 0
	v_cvt_pk_fp8_f32 v133, v139, v149 op_sel:[0,0,1]
	ds_write_b128 v144, v[130:133] offset:33152
	s_waitcnt lgkmcnt(0)
	s_barrier
	ds_read_b128 v[130:133], v145 offset:32768
	s_cbranch_scc1 .LBB0_693
	v_cmp_lt_i32_e32 vcc, s47, v138
	v_lshlrev_b32_e32 v0, 1, v138
	v_and_b32_e32 v139, 0x7f, v138
	s_and_saveexec_b64 s[6:7], vcc
	s_xor_b64 s[6:7], exec, s[6:7]
	v_add_u32_e32 v0, 0x7ffff800, v0
	v_and_b32_e32 v0, 0x7fffff00, v0
	v_or3_b32 v138, v139, v0, s64
	s_andn2_saveexec_b64 s[6:7], s[6:7]
	v_and_or_b32 v138, v0, s65, v139
	s_or_b64 exec, exec, s[6:7]

.LBB0_922:
	s_andn2_b64 vcc, exec, s[54:55]
	s_mov_b32 s43, 0
	s_cbranch_vccnz .LBB0_924
	s_and_b64 s[6:7], s[4:5], exec
	s_movk_i32 s6, 0x546
	s_cselect_b32 s6, s6, 0x1321
	v_readlane_b32 s7, v254, 41
	s_add_i32 s43, s6, s7

.Lcvp3_a_ready:
	v_mul_f32_e32 v0, 0x42800000, v2
	v_mul_f32_e32 v131, 0x42800000, v6
	v_mov_b32_e32 v130, v1
	v_cvt_pk_fp8_f32 v130, v0, v131
	v_mul_f32_e32 v132, 0x42800000, v10
	v_mul_f32_e32 v133, 0x42800000, v14
	v_mul_f32_e32 v0, 0x42800000, v18
	v_cvt_pk_fp8_f32 v130, v132, v133 op_sel:[0,0,1]
	v_mul_f32_e32 v132, 0x42800000, v22
	v_mov_b32_e32 v131, v1
	v_cvt_pk_fp8_f32 v131, v0, v132
	v_mul_f32_e32 v133, 0x42800000, v26
	v_mul_f32_e32 v138, 0x42800000, v30
	v_mul_f32_e32 v0, 0x42800000, v34
	v_cvt_pk_fp8_f32 v131, v133, v138 op_sel:[0,0,1]
	v_mul_f32_e32 v133, 0x42800000, v38
	v_mov_b32_e32 v132, v1
	v_cvt_pk_fp8_f32 v132, v0, v133
	v_mul_f32_e32 v138, 0x42800000, v42
	v_mul_f32_e32 v139, 0x42800000, v46
	v_mul_f32_e32 v0, 0x42800000, v50
	v_cvt_pk_fp8_f32 v132, v138, v139 op_sel:[0,0,1]
	v_mul_f32_e32 v138, 0x42800000, v54
	v_mov_b32_e32 v133, v1
	v_cvt_pk_fp8_f32 v133, v0, v138
	v_mul_f32_e32 v139, 0x42800000, v58
	v_mul_f32_e32 v149, 0x42800000, v62
	v_mul_f32_e32 v0, 0x42800000, v3
	v_cvt_pk_fp8_f32 v133, v139, v149 op_sel:[0,0,1]
	v_mul_f32_e32 v138, 0x42800000, v31
	v_mul_f32_e32 v139, 0x42800000, v47
	v_mul_f32_e32 v149, 0x42800000, v63
	ds_write_b128 v144, v[130:133]
	v_mul_f32_e32 v131, 0x42800000, v7
	v_mov_b32_e32 v130, v1
	v_cvt_pk_fp8_f32 v130, v0, v131
	v_mul_f32_e32 v132, 0x42800000, v11
	v_mul_f32_e32 v133, 0x42800000, v15
	v_mul_f32_e32 v0, 0x42800000, v19
	v_cvt_pk_fp8_f32 v130, v132, v133 op_sel:[0,0,1]
	v_mul_f32_e32 v132, 0x42800000, v23
	v_mov_b32_e32 v131, v1
	v_cvt_pk_fp8_f32 v131, v0, v132
	v_mul_f32_e32 v133, 0x42800000, v27
	v_mul_f32_e32 v0, 0x42800000, v35
	v_mov_b32_e32 v132, v1
	v_cvt_pk_fp8_f32 v131, v133, v138 op_sel:[0,0,1]
	v_mul_f32_e32 v133, 0x42800000, v39
	v_cvt_pk_fp8_f32 v132, v0, v133
	v_mul_f32_e32 v138, 0x42800000, v43
	v_mul_f32_e32 v0, 0x42800000, v51
	v_mov_b32_e32 v133, v1
	v_cvt_pk_fp8_f32 v132, v138, v139 op_sel:[0,0,1]
	v_mul_f32_e32 v138, 0x42800000, v55
	v_cvt_pk_fp8_f32 v133, v0, v138
	v_mul_f32_e32 v139, 0x42800000, v59
	v_mul_f32_e32 v0, 0x42800000, v4
	v_mul_f32_e32 v138, 0x42800000, v32
	v_cvt_pk_fp8_f32 v133, v139, v149 op_sel:[0,0,1]
	v_mul_f32_e32 v139, 0x42800000, v48
	v_mul_f32_e32 v149, 0x42800000, v64
	s_cmp_lg_u32 s34, 0
	ds_write_b128 v144, v[130:133] offset:128
	v_mul_f32_e32 v131, 0x42800000, v8
	v_mov_b32_e32 v130, v1
	v_cvt_pk_fp8_f32 v130, v0, v131
	v_mul_f32_e32 v132, 0x42800000, v12
	v_mul_f32_e32 v133, 0x42800000, v16
	v_mul_f32_e32 v0, 0x42800000, v20
	v_cvt_pk_fp8_f32 v130, v132, v133 op_sel:[0,0,1]
	v_mul_f32_e32 v132, 0x42800000, v24
	v_mov_b32_e32 v131, v1
	v_cvt_pk_fp8_f32 v131, v0, v132
	v_mul_f32_e32 v133, 0x42800000, v28
	v_mul_f32_e32 v0, 0x42800000, v36
	v_mov_b32_e32 v132, v1
	v_cvt_pk_fp8_f32 v131, v133, v138 op_sel:[0,0,1]
	v_mul_f32_e32 v133, 0x42800000, v40
	v_cvt_pk_fp8_f32 v132, v0, v133
	v_mul_f32_e32 v138, 0x42800000, v44
	v_mul_f32_e32 v0, 0x42800000, v52
	v_mov_b32_e32 v133, v1
	v_cvt_pk_fp8_f32 v132, v138, v139 op_sel:[0,0,1]
	v_mul_f32_e32 v138, 0x42800000, v56
	v_cvt_pk_fp8_f32 v133, v0, v138
	v_mul_f32_e32 v139, 0x42800000, v60
	v_mul_f32_e32 v0, 0x42800000, v5
	v_mul_f32_e32 v138, 0x42800000, v33
	v_cvt_pk_fp8_f32 v133, v139, v149 op_sel:[0,0,1]
	v_mul_f32_e32 v139, 0x42800000, v49
	v_mul_f32_e32 v149, 0x42800000, v65
	s_cselect_b64 s[20:21], -1, 0
	ds_write_b128 v144, v[130:133] offset:256
	v_mul_f32_e32 v131, 0x42800000, v9
	v_mov_b32_e32 v130, v1
	v_cvt_pk_fp8_f32 v130, v0, v131
	v_mul_f32_e32 v132, 0x42800000, v13
	v_mul_f32_e32 v133, 0x42800000, v17
	v_mul_f32_e32 v0, 0x42800000, v21
	v_cvt_pk_fp8_f32 v130, v132, v133 op_sel:[0,0,1]
	v_mul_f32_e32 v132, 0x42800000, v25
	v_mov_b32_e32 v131, v1
	v_cvt_pk_fp8_f32 v131, v0, v132
	v_mul_f32_e32 v133, 0x42800000, v29
	v_mul_f32_e32 v0, 0x42800000, v37
	v_mov_b32_e32 v132, v1
	v_cvt_pk_fp8_f32 v131, v133, v138 op_sel:[0,0,1]
	v_mul_f32_e32 v133, 0x42800000, v41
	v_cvt_pk_fp8_f32 v132, v0, v133
	v_mul_f32_e32 v138, 0x42800000, v45
	v_mul_f32_e32 v0, 0x42800000, v53
	v_mov_b32_e32 v133, v1
	v_cvt_pk_fp8_f32 v132, v138, v139 op_sel:[0,0,1]
	v_mul_f32_e32 v138, 0x42800000, v57
	v_cvt_pk_fp8_f32 v133, v0, v138
	v_mul_f32_e32 v139, 0x42800000, v61
	v_add_u32_e32 v138, s8, v140
	s_cmp_eq_u32 s34, 0
	v_cvt_pk_fp8_f32 v133, v139, v149 op_sel:[0,0,1]
	ds_write_b128 v144, v[130:133] offset:384
	s_waitcnt lgkmcnt(0)
	s_barrier
	ds_read_b128 v[130:133], v145
	s_cbranch_scc1 .LBB0_1429
	v_cmp_lt_i32_e32 vcc, s47, v138
	v_lshlrev_b32_e32 v0, 1, v138
	v_and_b32_e32 v139, 0x7f, v138
	s_and_saveexec_b64 s[6:7], vcc
	s_xor_b64 s[6:7], exec, s[6:7]
	v_add_u32_e32 v0, 0x7ffff800, v0
	v_and_b32_e32 v0, 0x7fffff00, v0
	v_or3_b32 v138, v139, v0, s64
	s_andn2_saveexec_b64 s[6:7], s[6:7]
	v_and_or_b32 v138, v0, s65, v139
	s_or_b64 exec, exec, s[6:7]

.LBB0_1455:
	s_waitcnt vmcnt(0)
.Lcvp3_b_ready:
	v_mul_f32_e32 v0, 0x42800000, v70
	v_mul_f32_e32 v131, 0x42800000, v66
	v_mov_b32_e32 v130, v1
	v_cvt_pk_fp8_f32 v130, v0, v131
	v_mul_f32_e32 v132, 0x42800000, v78
	v_mul_f32_e32 v133, 0x42800000, v74
	v_mul_f32_e32 v0, 0x42800000, v86
	v_cvt_pk_fp8_f32 v130, v132, v133 op_sel:[0,0,1]
	v_mul_f32_e32 v132, 0x42800000, v82
	v_mov_b32_e32 v131, v1
	v_cvt_pk_fp8_f32 v131, v0, v132
	v_mul_f32_e32 v133, 0x42800000, v94
	v_mul_f32_e32 v138, 0x42800000, v90
	v_mul_f32_e32 v0, 0x42800000, v98
	v_cvt_pk_fp8_f32 v131, v133, v138 op_sel:[0,0,1]
	v_mul_f32_e32 v133, 0x42800000, v102
	v_mov_b32_e32 v132, v1
	v_cvt_pk_fp8_f32 v132, v0, v133
	v_mul_f32_e32 v138, 0x42800000, v106
	v_mul_f32_e32 v139, 0x42800000, v110
	v_mul_f32_e32 v0, 0x42800000, v114
	v_cvt_pk_fp8_f32 v132, v138, v139 op_sel:[0,0,1]
	v_mul_f32_e32 v138, 0x42800000, v118
	v_mov_b32_e32 v133, v1
	v_cvt_pk_fp8_f32 v133, v0, v138
	v_mul_f32_e32 v139, 0x42800000, v122
	v_mul_f32_e32 v149, 0x42800000, v126
	v_mul_f32_e32 v0, 0x42800000, v71
	v_cvt_pk_fp8_f32 v133, v139, v149 op_sel:[0,0,1]
	v_mul_f32_e32 v138, 0x42800000, v91
	v_mul_f32_e32 v139, 0x42800000, v111
	v_mul_f32_e32 v149, 0x42800000, v127
	ds_write_b128 v144, v[130:133] offset:32768
	v_mul_f32_e32 v131, 0x42800000, v67
	v_mov_b32_e32 v130, v1
	v_cvt_pk_fp8_f32 v130, v0, v131
	v_mul_f32_e32 v132, 0x42800000, v79
	v_mul_f32_e32 v133, 0x42800000, v75
	v_mul_f32_e32 v0, 0x42800000, v87
	v_cvt_pk_fp8_f32 v130, v132, v133 op_sel:[0,0,1]
	v_mul_f32_e32 v132, 0x42800000, v83
	v_mov_b32_e32 v131, v1
	v_cvt_pk_fp8_f32 v131, v0, v132
	v_mul_f32_e32 v133, 0x42800000, v95
	v_mul_f32_e32 v0, 0x42800000, v99
	v_mov_b32_e32 v132, v1
	v_cvt_pk_fp8_f32 v131, v133, v138 op_sel:[0,0,1]
	v_mul_f32_e32 v133, 0x42800000, v103
	v_cvt_pk_fp8_f32 v132, v0, v133
	v_mul_f32_e32 v138, 0x42800000, v107
	v_mul_f32_e32 v0, 0x42800000, v115
	v_mov_b32_e32 v133, v1
	v_cvt_pk_fp8_f32 v132, v138, v139 op_sel:[0,0,1]
	v_mul_f32_e32 v138, 0x42800000, v119
	v_cvt_pk_fp8_f32 v133, v0, v138
	v_mul_f32_e32 v139, 0x42800000, v123
	v_mul_f32_e32 v0, 0x42800000, v72
	v_mul_f32_e32 v138, 0x42800000, v92
	v_cvt_pk_fp8_f32 v133, v139, v149 op_sel:[0,0,1]
	v_mul_f32_e32 v139, 0x42800000, v112
	v_mul_f32_e32 v149, 0x42800000, v128
	s_cmp_lg_u32 s37, 0
	ds_write_b128 v144, v[130:133] offset:32896
	v_mul_f32_e32 v131, 0x42800000, v68
	v_mov_b32_e32 v130, v1
	v_cvt_pk_fp8_f32 v130, v0, v131
	v_mul_f32_e32 v132, 0x42800000, v80
	v_mul_f32_e32 v133, 0x42800000, v76
	v_mul_f32_e32 v0, 0x42800000, v88
	v_cvt_pk_fp8_f32 v130, v132, v133 op_sel:[0,0,1]
	v_mul_f32_e32 v132, 0x42800000, v84
	v_mov_b32_e32 v131, v1
	v_cvt_pk_fp8_f32 v131, v0, v132
	v_mul_f32_e32 v133, 0x42800000, v96
	v_mul_f32_e32 v0, 0x42800000, v100
	v_mov_b32_e32 v132, v1
	v_cvt_pk_fp8_f32 v131, v133, v138 op_sel:[0,0,1]
	v_mul_f32_e32 v133, 0x42800000, v104
	v_cvt_pk_fp8_f32 v132, v0, v133
	v_mul_f32_e32 v138, 0x42800000, v108
	v_mul_f32_e32 v0, 0x42800000, v116
	v_mov_b32_e32 v133, v1
	v_cvt_pk_fp8_f32 v132, v138, v139 op_sel:[0,0,1]
	v_mul_f32_e32 v138, 0x42800000, v120
	v_cvt_pk_fp8_f32 v133, v0, v138
	v_mul_f32_e32 v139, 0x42800000, v124
	v_mul_f32_e32 v0, 0x42800000, v73
	v_mul_f32_e32 v138, 0x42800000, v93
	v_cvt_pk_fp8_f32 v133, v139, v149 op_sel:[0,0,1]
	v_mul_f32_e32 v139, 0x42800000, v113
	v_mul_f32_e32 v149, 0x42800000, v129
	s_cselect_b64 s[18:19], -1, 0
	ds_write_b128 v144, v[130:133] offset:33024
	v_mul_f32_e32 v131, 0x42800000, v69
	v_mov_b32_e32 v130, v1
	v_cvt_pk_fp8_f32 v130, v0, v131
	v_mul_f32_e32 v132, 0x42800000, v81
	v_mul_f32_e32 v133, 0x42800000, v77
	v_mul_f32_e32 v0, 0x42800000, v89
	v_cvt_pk_fp8_f32 v130, v132, v133 op_sel:[0,0,1]
	v_mul_f32_e32 v132, 0x42800000, v85
	v_mov_b32_e32 v131, v1
	v_cvt_pk_fp8_f32 v131, v0, v132
	v_mul_f32_e32 v133, 0x42800000, v97
	v_mul_f32_e32 v0, 0x42800000, v101
	v_mov_b32_e32 v132, v1
	v_cvt_pk_fp8_f32 v131, v133, v138 op_sel:[0,0,1]
	v_mul_f32_e32 v133, 0x42800000, v105
	v_cvt_pk_fp8_f32 v132, v0, v133
	v_mul_f32_e32 v138, 0x42800000, v109
	v_mul_f32_e32 v0, 0x42800000, v117
	v_mov_b32_e32 v133, v1
	v_cvt_pk_fp8_f32 v132, v138, v139 op_sel:[0,0,1]
	v_mul_f32_e32 v138, 0x42800000, v121
	v_cvt_pk_fp8_f32 v133, v0, v138
	v_mul_f32_e32 v139, 0x42800000, v125
	v_add_u32_e32 v138, s12, v140
	s_cmp_eq_u32 s37, 0
	v_cvt_pk_fp8_f32 v133, v139, v149 op_sel:[0,0,1]
	ds_write_b128 v144, v[130:133] offset:33152
	s_waitcnt lgkmcnt(0)
	s_barrier
	ds_read_b128 v[130:133], v145 offset:32768
	s_cbranch_scc1 .LBB0_1461
	v_cmp_lt_i32_e32 vcc, s47, v138
	v_lshlrev_b32_e32 v0, 1, v138
	v_and_b32_e32 v139, 0x7f, v138
	s_and_saveexec_b64 s[6:7], vcc
	s_xor_b64 s[6:7], exec, s[6:7]
	v_add_u32_e32 v0, 0x7ffff800, v0
	v_and_b32_e32 v0, 0x7fffff00, v0
	v_or3_b32 v138, v139, v0, s64
	s_andn2_saveexec_b64 s[6:7], s[6:7]
	v_and_or_b32 v138, v0, s65, v139
	s_or_b64 exec, exec, s[6:7]
